# early L2 write-back by the 24th of 32 arrivers per XCD at each grid barrier
# speedup vs baseline: 1.0121x; 1.0003x over previous
; __device__ __forceinline__ unsigned xb_ld(unsigned* p)              { return __hip_atomic_load(p, __ATOMIC_RELAXED, __HIP_MEMORY_SCOPE_AGENT); }
; __device__ __forceinline__ unsigned xb_add(unsigned* p, unsigned v) { return __hip_atomic_fetch_add(p, v, __ATOMIC_RELAXED, __HIP_MEMORY_SCOPE_AGENT); }
; #define XB_SPIN(cond, bar) do { unsigned _sp = 0; while (cond) { __builtin_amdgcn_s_sleep(1); \
;     if ((++_sp & 255u) == 0u) { if (xb_ld(&(bar)[XB_TMO])) break; if (_sp > XB_SPIN_CAP) { atomicAdd(&(bar)[XB_TMO], 1u); break; } } } } while (0)
; __device__ __forceinline__ void xcd_barrier(const XcdBarrier& b, bool t0) {
;     ...
;         const unsigned old = xb_add(&bar[XB_XSUB(b.x)], 1u);
;         const unsigned gen = old / nloc;
;         if (old + 1u == (gen + 1u) * nloc) {
;             __builtin_amdgcn_fence(__ATOMIC_RELEASE, "agent");
;             asm volatile("s_waitcnt vmcnt(0)" ::: "memory");
;             const unsigned og = xb_add(&bar[XB_TOP], 1u);
;             const unsigned tg = og / nx;
;             if (og + 1u == (tg + 1u) * nx) xb_add(&bar[XB_TOPGEN], 1u);
;             else XB_SPIN(xb_ld(&bar[XB_TOPGEN]) == tg, bar);
;             __builtin_amdgcn_fence(__ATOMIC_ACQUIRE, "agent");
;             xb_add(&bar[XB_XGEN(b.x)], 1u);
;             asm volatile("s_waitcnt vmcnt(0)" ::: "memory");
;         } else {
;             XB_SPIN(xb_ld(&bar[XB_XGEN(b.x)]) == gen, bar);
.LBB0_214:
	v_readlane_b32 s3, v254, 45
	s_lshl_b32 s3, s3, 8
	v_readlane_b32 s6, v254, 43
	v_readlane_b32 s7, v254, 44
	s_add_u32 s6, s6, s3
	s_addc_u32 s7, s7, 0
	v_mov_b32_e32 v1, 0x1000
	v_mov_b32_e32 v3, 1
	v_sub_u32_e32 v4, 0, v2
	global_atomic_add v3, v1, v3, s[6:7] offset:1024 sc0
	v_cvt_f32_u32_e32 v1, v2
	v_rcp_iflag_f32_e32 v1, v1
	s_nop 0
	v_mul_f32_e32 v1, 0x4f7ffffe, v1
	v_cvt_u32_f32_e32 v1, v1
	v_mul_lo_u32 v4, v4, v1
	v_mul_hi_u32 v4, v1, v4
	v_add_u32_e32 v1, v1, v4
	s_waitcnt vmcnt(0)
	v_mul_hi_u32 v1, v3, v1
	v_mul_lo_u32 v4, v1, v2
	v_sub_u32_e32 v4, v3, v4
	v_add_u32_e32 v5, 1, v1
	v_cmp_ge_u32_e32 vcc, v4, v2
	v_add_u32_e32 v3, 1, v3
	s_nop 0
	v_cndmask_b32_e32 v1, v1, v5, vcc
	v_sub_u32_e32 v5, v4, v2
	v_cndmask_b32_e32 v4, v4, v5, vcc
	v_add_u32_e32 v5, 1, v1
	v_cmp_ge_u32_e32 vcc, v4, v2
	s_nop 1
	v_cndmask_b32_e32 v1, v1, v5, vcc
	v_mul_lo_u32 v4, v2, v1
	v_add_u32_e32 v2, v4, v2
	v_cmp_ne_u32_e32 vcc, v3, v2
	s_and_saveexec_b64 s[8:9], vcc
	s_xor_b64 s[8:9], exec, s[8:9]
	s_cbranch_execz .LBB0_228
	v_sub_u32_e32 v5, v2, v4
	v_sub_u32_e32 v3, v3, v4
	v_lshrrev_b32_e32 v4, 2, v5
	v_sub_u32_e32 v5, v5, v4
	v_cmp_ne_u32_e32 vcc, v3, v5
	s_cbranch_vccnz .Lef_skip_1
	buffer_wbl2 sc1
	s_waitcnt vmcnt(0)
.Lef_skip_1:
	s_waitcnt lgkmcnt(0)
	v_mov_b32_e32 v0, 0x2000
	global_load_dword v0, v0, s[6:7] offset:1024 sc1
	s_add_u32 s14, s6, 0x2400
	s_addc_u32 s15, s7, 0
	s_waitcnt vmcnt(0)
	v_cmp_eq_u32_e32 vcc, v0, v1
	s_and_saveexec_b64 s[10:11], vcc
	s_cbranch_execz .LBB0_227
	s_add_u32 s12, s46, 0x4200
	s_addc_u32 s13, s47, 0
	s_mov_b32 s3, 1
	s_mov_b64 s[16:17], 0
	v_mov_b32_e32 v0, 0
	s_branch .LBB0_218

; __device__ __forceinline__ unsigned xb_ld(unsigned* p)              { return __hip_atomic_load(p, __ATOMIC_RELAXED, __HIP_MEMORY_SCOPE_AGENT); }
; __device__ __forceinline__ unsigned xb_add(unsigned* p, unsigned v) { return __hip_atomic_fetch_add(p, v, __ATOMIC_RELAXED, __HIP_MEMORY_SCOPE_AGENT); }
; #define XB_SPIN(cond, bar) do { unsigned _sp = 0; while (cond) { __builtin_amdgcn_s_sleep(1); \
;     if ((++_sp & 255u) == 0u) { if (xb_ld(&(bar)[XB_TMO])) break; if (_sp > XB_SPIN_CAP) { atomicAdd(&(bar)[XB_TMO], 1u); break; } } } } while (0)
; __device__ __forceinline__ void xcd_barrier(const XcdBarrier& b, bool t0) {
;     ...
;         const unsigned old = xb_add(&bar[XB_XSUB(b.x)], 1u);
;         const unsigned gen = old / nloc;
;         if (old + 1u == (gen + 1u) * nloc) {
;             __builtin_amdgcn_fence(__ATOMIC_RELEASE, "agent");
;             asm volatile("s_waitcnt vmcnt(0)" ::: "memory");
;             const unsigned og = xb_add(&bar[XB_TOP], 1u);
;             const unsigned tg = og / nx;
;             if (og + 1u == (tg + 1u) * nx) xb_add(&bar[XB_TOPGEN], 1u);
;             else XB_SPIN(xb_ld(&bar[XB_TOPGEN]) == tg, bar);
;             __builtin_amdgcn_fence(__ATOMIC_ACQUIRE, "agent");
;             xb_add(&bar[XB_XGEN(b.x)], 1u);
;             asm volatile("s_waitcnt vmcnt(0)" ::: "memory");
;         } else {
;             XB_SPIN(xb_ld(&bar[XB_XGEN(b.x)]) == gen, bar);
.LBB0_479:
	v_readlane_b32 s3, v254, 45
	s_lshl_b32 s3, s3, 8
	v_readlane_b32 s6, v254, 43
	v_readlane_b32 s7, v254, 44
	s_add_u32 s6, s6, s3
	s_addc_u32 s7, s7, 0
	v_mov_b32_e32 v1, 0x1000
	v_mov_b32_e32 v4, 1
	v_sub_u32_e32 v5, 0, v3
	global_atomic_add v4, v1, v4, s[6:7] offset:1024 sc0
	v_cvt_f32_u32_e32 v1, v3
	v_rcp_iflag_f32_e32 v1, v1
	s_nop 0
	v_mul_f32_e32 v1, 0x4f7ffffe, v1
	v_cvt_u32_f32_e32 v1, v1
	v_mul_lo_u32 v5, v5, v1
	v_mul_hi_u32 v5, v1, v5
	v_add_u32_e32 v1, v1, v5
	s_waitcnt vmcnt(0)
	v_mul_hi_u32 v1, v4, v1
	v_mul_lo_u32 v5, v1, v3
	v_sub_u32_e32 v5, v4, v5
	v_add_u32_e32 v6, 1, v1
	v_cmp_ge_u32_e32 vcc, v5, v3
	v_add_u32_e32 v4, 1, v4
	s_nop 0
	v_cndmask_b32_e32 v1, v1, v6, vcc
	v_sub_u32_e32 v6, v5, v3
	v_cndmask_b32_e32 v5, v5, v6, vcc
	v_add_u32_e32 v6, 1, v1
	v_cmp_ge_u32_e32 vcc, v5, v3
	s_nop 1
	v_cndmask_b32_e32 v1, v1, v6, vcc
	v_mul_lo_u32 v5, v3, v1
	v_add_u32_e32 v3, v5, v3
	v_cmp_ne_u32_e32 vcc, v4, v3
	s_and_saveexec_b64 s[8:9], vcc
	s_xor_b64 s[8:9], exec, s[8:9]
	s_cbranch_execz .LBB0_493
	v_sub_u32_e32 v6, v3, v5
	v_sub_u32_e32 v4, v4, v5
	v_lshrrev_b32_e32 v5, 2, v6
	v_sub_u32_e32 v6, v6, v5
	v_cmp_ne_u32_e32 vcc, v4, v6
	s_cbranch_vccnz .Lef_skip_3
	buffer_wbl2 sc1
	s_waitcnt vmcnt(0)

; __device__ __forceinline__ unsigned xb_ld(unsigned* p)              { return __hip_atomic_load(p, __ATOMIC_RELAXED, __HIP_MEMORY_SCOPE_AGENT); }
; __device__ __forceinline__ unsigned xb_add(unsigned* p, unsigned v) { return __hip_atomic_fetch_add(p, v, __ATOMIC_RELAXED, __HIP_MEMORY_SCOPE_AGENT); }
; #define XB_SPIN(cond, bar) do { unsigned _sp = 0; while (cond) { __builtin_amdgcn_s_sleep(1); \
;     if ((++_sp & 255u) == 0u) { if (xb_ld(&(bar)[XB_TMO])) break; if (_sp > XB_SPIN_CAP) { atomicAdd(&(bar)[XB_TMO], 1u); break; } } } } while (0)
; __device__ __forceinline__ void xcd_barrier(const XcdBarrier& b, bool t0) {
;     ...
;         const unsigned old = xb_add(&bar[XB_XSUB(b.x)], 1u);
;         const unsigned gen = old / nloc;
;         if (old + 1u == (gen + 1u) * nloc) {
;             __builtin_amdgcn_fence(__ATOMIC_RELEASE, "agent");
;             asm volatile("s_waitcnt vmcnt(0)" ::: "memory");
;             const unsigned og = xb_add(&bar[XB_TOP], 1u);
;             const unsigned tg = og / nx;
;             if (og + 1u == (tg + 1u) * nx) xb_add(&bar[XB_TOPGEN], 1u);
;             else XB_SPIN(xb_ld(&bar[XB_TOPGEN]) == tg, bar);
;             __builtin_amdgcn_fence(__ATOMIC_ACQUIRE, "agent");
;             xb_add(&bar[XB_XGEN(b.x)], 1u);
;             asm volatile("s_waitcnt vmcnt(0)" ::: "memory");
;         } else {
;             XB_SPIN(xb_ld(&bar[XB_XGEN(b.x)]) == gen, bar);
.LBB0_534:
	v_readlane_b32 s3, v254, 45
	s_lshl_b32 s3, s3, 8
	v_readlane_b32 s6, v254, 43
	v_readlane_b32 s7, v254, 44
	s_add_u32 s6, s6, s3
	s_addc_u32 s7, s7, 0
	v_mov_b32_e32 v1, 0x1000
	v_mov_b32_e32 v5, 1
	v_sub_u32_e32 v6, 0, v4
	global_atomic_add v5, v1, v5, s[6:7] offset:1024 sc0
	v_cvt_f32_u32_e32 v1, v4
	v_rcp_iflag_f32_e32 v1, v1
	s_nop 0
	v_mul_f32_e32 v1, 0x4f7ffffe, v1
	v_cvt_u32_f32_e32 v1, v1
	v_mul_lo_u32 v6, v6, v1
	v_mul_hi_u32 v6, v1, v6
	v_add_u32_e32 v1, v1, v6
	s_waitcnt vmcnt(0)
	v_mul_hi_u32 v1, v5, v1
	v_mul_lo_u32 v6, v1, v4
	v_sub_u32_e32 v6, v5, v6
	v_add_u32_e32 v7, 1, v1
	v_cmp_ge_u32_e32 vcc, v6, v4
	v_add_u32_e32 v5, 1, v5
	s_nop 0
	v_cndmask_b32_e32 v1, v1, v7, vcc
	v_sub_u32_e32 v7, v6, v4
	v_cndmask_b32_e32 v6, v6, v7, vcc
	v_add_u32_e32 v7, 1, v1
	v_cmp_ge_u32_e32 vcc, v6, v4
	s_nop 1
	v_cndmask_b32_e32 v1, v1, v7, vcc
	v_mul_lo_u32 v6, v4, v1
	v_add_u32_e32 v4, v6, v4
	v_cmp_ne_u32_e32 vcc, v5, v4
	s_and_saveexec_b64 s[8:9], vcc
	s_xor_b64 s[8:9], exec, s[8:9]
	s_cbranch_execz .LBB0_548
	v_sub_u32_e32 v7, v4, v6
	v_sub_u32_e32 v5, v5, v6
	v_lshrrev_b32_e32 v6, 2, v7
	v_sub_u32_e32 v7, v7, v6
	v_cmp_ne_u32_e32 vcc, v5, v7
	s_cbranch_vccnz .Lef_skip_4
	buffer_wbl2 sc1
	s_waitcnt vmcnt(0)

; __device__ __forceinline__ unsigned xb_ld(unsigned* p)              { return __hip_atomic_load(p, __ATOMIC_RELAXED, __HIP_MEMORY_SCOPE_AGENT); }
; __device__ __forceinline__ unsigned xb_add(unsigned* p, unsigned v) { return __hip_atomic_fetch_add(p, v, __ATOMIC_RELAXED, __HIP_MEMORY_SCOPE_AGENT); }
; #define XB_SPIN(cond, bar) do { unsigned _sp = 0; while (cond) { __builtin_amdgcn_s_sleep(1); \
;     if ((++_sp & 255u) == 0u) { if (xb_ld(&(bar)[XB_TMO])) break; if (_sp > XB_SPIN_CAP) { atomicAdd(&(bar)[XB_TMO], 1u); break; } } } } while (0)
; __device__ __forceinline__ void xcd_barrier(const XcdBarrier& b, bool t0) {
;     ...
;         const unsigned old = xb_add(&bar[XB_XSUB(b.x)], 1u);
;         const unsigned gen = old / nloc;
;         if (old + 1u == (gen + 1u) * nloc) {
;             __builtin_amdgcn_fence(__ATOMIC_RELEASE, "agent");
;             asm volatile("s_waitcnt vmcnt(0)" ::: "memory");
;             const unsigned og = xb_add(&bar[XB_TOP], 1u);
;             const unsigned tg = og / nx;
;             if (og + 1u == (tg + 1u) * nx) xb_add(&bar[XB_TOPGEN], 1u);
;             else XB_SPIN(xb_ld(&bar[XB_TOPGEN]) == tg, bar);
;             __builtin_amdgcn_fence(__ATOMIC_ACQUIRE, "agent");
;             xb_add(&bar[XB_XGEN(b.x)], 1u);
;             asm volatile("s_waitcnt vmcnt(0)" ::: "memory");
;         } else {
;             XB_SPIN(xb_ld(&bar[XB_XGEN(b.x)]) == gen, bar);
.LBB0_1646:
	v_readlane_b32 s3, v254, 45
	s_lshl_b32 s3, s3, 8
	v_readlane_b32 s4, v254, 43
	v_readlane_b32 s5, v254, 44
	s_add_u32 s4, s4, s3
	s_addc_u32 s5, s5, 0
	v_mov_b32_e32 v1, 0x1000
	v_mov_b32_e32 v3, 1
	v_sub_u32_e32 v4, 0, v2
	global_atomic_add v3, v1, v3, s[4:5] offset:1024 sc0
	v_cvt_f32_u32_e32 v1, v2
	v_rcp_iflag_f32_e32 v1, v1
	s_nop 0
	v_mul_f32_e32 v1, 0x4f7ffffe, v1
	v_cvt_u32_f32_e32 v1, v1
	v_mul_lo_u32 v4, v4, v1
	v_mul_hi_u32 v4, v1, v4
	v_add_u32_e32 v1, v1, v4
	s_waitcnt vmcnt(0)
	v_mul_hi_u32 v1, v3, v1
	v_mul_lo_u32 v4, v1, v2
	v_sub_u32_e32 v4, v3, v4
	v_add_u32_e32 v5, 1, v1
	v_cmp_ge_u32_e32 vcc, v4, v2
	v_add_u32_e32 v3, 1, v3
	s_nop 0
	v_cndmask_b32_e32 v1, v1, v5, vcc
	v_sub_u32_e32 v5, v4, v2
	v_cndmask_b32_e32 v4, v4, v5, vcc
	v_add_u32_e32 v5, 1, v1
	v_cmp_ge_u32_e32 vcc, v4, v2
	s_nop 1
	v_cndmask_b32_e32 v1, v1, v5, vcc
	v_mul_lo_u32 v4, v2, v1
	v_add_u32_e32 v2, v4, v2
	v_cmp_ne_u32_e32 vcc, v3, v2
	s_and_saveexec_b64 s[6:7], vcc
	s_xor_b64 s[6:7], exec, s[6:7]
	s_cbranch_execz .LBB0_1660
	v_sub_u32_e32 v5, v2, v4
	v_sub_u32_e32 v3, v3, v4
	v_lshrrev_b32_e32 v4, 2, v5
	v_sub_u32_e32 v5, v5, v4
	v_cmp_ne_u32_e32 vcc, v3, v5
	s_cbranch_vccnz .Lef_skip_11
	buffer_wbl2 sc1
	s_waitcnt vmcnt(0)
.Lef_skip_11:
	s_waitcnt lgkmcnt(0)
	v_mov_b32_e32 v0, 0x2000
	global_load_dword v0, v0, s[4:5] offset:1024 sc1
	s_add_u32 s12, s4, 0x2400
	s_addc_u32 s13, s5, 0
	s_waitcnt vmcnt(0)
	v_cmp_eq_u32_e32 vcc, v0, v1
	s_and_saveexec_b64 s[8:9], vcc
	s_cbranch_execz .LBB0_1659
	s_add_u32 s10, s46, 0x4200
	s_addc_u32 s11, s47, 0
	s_mov_b32 s3, 1
	s_mov_b64 s[14:15], 0
	v_mov_b32_e32 v0, 0
	s_branch .LBB0_1650
